# topk score tile: all q/K loads batched in line-major order with counted waits, MFMAs consume in load order (same per-accumulator sum order)
# speedup vs baseline: 1.0183x; 1.0183x over previous
.LBB0_922:
	s_xor_b64 s[12:13], s[16:17], -1
	v_lshl_add_u64 v[80:81], s[14:15], 1, v[72:73]
	s_and_b64 s[14:15], s[16:17], exec
	s_mov_b32 s14, 0x100000
	s_cselect_b32 s84, s14, 0x180000
	v_lshl_add_u64 v[78:79], v[74:75], 0, s[84:85]
	v_add_co_u32_e32 v86, vcc, 0x2000, v78
	s_mov_b32 s16, s7
	v_addc_co_u32_e32 v87, vcc, 0, v79, vcc
	v_add_co_u32_e32 v82, vcc, s29, v78
	s_nop 0
	v_addc_co_u32_e32 v83, vcc, 0, v79, vcc
	v_add_co_u32_e32 v84, vcc, 0x6000, v78
	s_nop 0
	v_addc_co_u32_e32 v85, vcc, 0, v79, vcc
	global_load_dwordx4 v[116:119], v[80:81], off nt
	global_load_dwordx4 v[120:123], v[80:81], off offset:32 nt
	global_load_dwordx4 v[130:133], v[80:81], off offset:64 nt
	global_load_dwordx4 v[134:137], v[80:81], off offset:96 nt
	global_load_dwordx4 v[138:141], v[78:79], off
	global_load_dwordx4 v[142:145], v[78:79], off offset:32
	global_load_dwordx4 v[146:149], v[78:79], off offset:64
	global_load_dwordx4 v[150:153], v[78:79], off offset:96
	global_load_dwordx4 v[154:157], v[86:87], off
	global_load_dwordx4 v[158:161], v[86:87], off offset:32
	global_load_dwordx4 v[162:165], v[86:87], off offset:64
	global_load_dwordx4 v[166:169], v[86:87], off offset:96
	global_load_dwordx4 v[170:173], v[82:83], off
	global_load_dwordx4 v[176:179], v[82:83], off offset:32
	global_load_dwordx4 v[180:183], v[82:83], off offset:64
	global_load_dwordx4 v[184:187], v[82:83], off offset:96
	global_load_dwordx4 v[188:191], v[84:85], off
	global_load_dwordx4 v[192:195], v[84:85], off offset:32
	global_load_dwordx4 v[196:199], v[84:85], off offset:64
	global_load_dwordx4 v[216:219], v[84:85], off offset:96
	global_load_dwordx4 v[220:223], v[80:81], off offset:128 nt
	global_load_dwordx4 v[224:227], v[80:81], off offset:160 nt
	global_load_dwordx4 v[228:231], v[80:81], off offset:192 nt
	global_load_dwordx4 v[232:235], v[80:81], off offset:224 nt
	global_load_dwordx4 v[236:239], v[78:79], off offset:128
	global_load_dwordx4 v[240:243], v[78:79], off offset:160
	global_load_dwordx4 v[244:247], v[78:79], off offset:192
	global_load_dwordx4 v[248:251], v[78:79], off offset:224
	s_waitcnt vmcnt(20)
	v_mfma_f32_32x32x16_bf16 v[6:21], v[116:119], v[138:141], 0
	v_mfma_f32_32x32x16_bf16 v[6:21], v[120:123], v[142:145], v[6:21]
	v_mfma_f32_32x32x16_bf16 v[6:21], v[130:133], v[146:149], v[6:21]
	v_mfma_f32_32x32x16_bf16 v[6:21], v[134:137], v[150:153], v[6:21]
	global_load_dwordx4 v[138:141], v[86:87], off offset:128
	global_load_dwordx4 v[142:145], v[86:87], off offset:160
	global_load_dwordx4 v[146:149], v[86:87], off offset:192
	global_load_dwordx4 v[150:153], v[86:87], off offset:224
	s_waitcnt vmcnt(20)
	v_mfma_f32_32x32x16_bf16 v[38:53], v[116:119], v[154:157], 0
	v_mfma_f32_32x32x16_bf16 v[38:53], v[120:123], v[158:161], v[38:53]
	v_mfma_f32_32x32x16_bf16 v[38:53], v[130:133], v[162:165], v[38:53]
	v_mfma_f32_32x32x16_bf16 v[38:53], v[134:137], v[166:169], v[38:53]
	global_load_dwordx4 v[154:157], v[82:83], off offset:128
	global_load_dwordx4 v[158:161], v[82:83], off offset:160
	global_load_dwordx4 v[162:165], v[82:83], off offset:192
	global_load_dwordx4 v[166:169], v[82:83], off offset:224
	s_waitcnt vmcnt(20)
	v_mfma_f32_32x32x16_bf16 v[22:37], v[116:119], v[170:173], 0
	v_mfma_f32_32x32x16_bf16 v[22:37], v[120:123], v[176:179], v[22:37]
	v_mfma_f32_32x32x16_bf16 v[22:37], v[130:133], v[180:183], v[22:37]
	v_mfma_f32_32x32x16_bf16 v[22:37], v[134:137], v[184:187], v[22:37]
	global_load_dwordx4 v[170:173], v[84:85], off offset:128
	global_load_dwordx4 v[176:179], v[84:85], off offset:160
	global_load_dwordx4 v[180:183], v[84:85], off offset:192
	global_load_dwordx4 v[184:187], v[84:85], off offset:224
	s_waitcnt vmcnt(20)
	v_mfma_f32_32x32x16_bf16 v[54:69], v[116:119], v[188:191], 0
	v_mfma_f32_32x32x16_bf16 v[54:69], v[120:123], v[192:195], v[54:69]
	v_mfma_f32_32x32x16_bf16 v[54:69], v[130:133], v[196:199], v[54:69]
	v_mfma_f32_32x32x16_bf16 v[54:69], v[134:137], v[216:219], v[54:69]
	s_waitcnt vmcnt(12)
	v_mfma_f32_32x32x16_bf16 v[6:21], v[220:223], v[236:239], v[6:21]
	v_mfma_f32_32x32x16_bf16 v[6:21], v[224:227], v[240:243], v[6:21]
	v_mfma_f32_32x32x16_bf16 v[6:21], v[228:231], v[244:247], v[6:21]
	v_mfma_f32_32x32x16_bf16 v[6:21], v[232:235], v[248:251], v[6:21]
	s_waitcnt vmcnt(8)
	v_mfma_f32_32x32x16_bf16 v[38:53], v[220:223], v[138:141], v[38:53]
	v_mfma_f32_32x32x16_bf16 v[38:53], v[224:227], v[142:145], v[38:53]
	v_mfma_f32_32x32x16_bf16 v[38:53], v[228:231], v[146:149], v[38:53]
	v_mfma_f32_32x32x16_bf16 v[38:53], v[232:235], v[150:153], v[38:53]
	s_waitcnt vmcnt(4)
	v_mfma_f32_32x32x16_bf16 v[22:37], v[220:223], v[154:157], v[22:37]
	v_mfma_f32_32x32x16_bf16 v[22:37], v[224:227], v[158:161], v[22:37]
	v_mfma_f32_32x32x16_bf16 v[22:37], v[228:231], v[162:165], v[22:37]
	v_mfma_f32_32x32x16_bf16 v[22:37], v[232:235], v[166:169], v[22:37]
	s_waitcnt vmcnt(0)
	v_mfma_f32_32x32x16_bf16 v[54:69], v[220:223], v[170:173], v[54:69]
	v_mfma_f32_32x32x16_bf16 v[54:69], v[224:227], v[176:179], v[54:69]
	v_mfma_f32_32x32x16_bf16 v[54:69], v[228:231], v[180:183], v[54:69]
	v_mfma_f32_32x32x16_bf16 v[54:69], v[232:235], v[184:187], v[54:69]
	s_nop 7
	ds_write2_b32 v93, v6, v38 offset1:32
	ds_write2_b32 v93, v7, v39 offset0:128 offset1:160
	v_add_u32_e32 v6, 0x400, v93
	ds_write2_b32 v6, v8, v40 offset1:32
	ds_write2_b32 v6, v9, v41 offset0:128 offset1:160
	v_add_u32_e32 v7, 0x1000, v93
	v_add_u32_e32 v8, 0x1400, v93
	ds_write2_b32 v7, v10, v42 offset1:32
	ds_write2_b32 v7, v11, v43 offset0:128 offset1:160
	ds_write2_b32 v8, v12, v44 offset1:32
	ds_write2_b32 v8, v13, v45 offset0:128 offset1:160
	v_add_u32_e32 v9, 0x2000, v93
	v_add_u32_e32 v10, 0x2400, v93
	v_add_u32_e32 v11, 0x3000, v93
	v_add_u32_e32 v12, 0x3400, v93
	ds_write2_b32 v9, v14, v46 offset1:32
	ds_write2_b32 v9, v15, v47 offset0:128 offset1:160
	ds_write2_b32 v10, v16, v48 offset1:32
	ds_write2_b32 v10, v17, v49 offset0:128 offset1:160
	ds_write2_b32 v11, v18, v50 offset1:32
	ds_write2_b32 v11, v19, v51 offset0:128 offset1:160
	v_mov_b32_e32 v13, v108
	v_mov_b32_e32 v14, v71
	ds_write2_b32 v12, v20, v52 offset1:32
	ds_write2_b32 v12, v21, v53 offset0:128 offset1:160
	s_nop 9
	ds_write2_b32 v93, v22, v54 offset0:64 offset1:96
	ds_write2_b32 v93, v23, v55 offset0:192 offset1:224
	ds_write2_b32 v6, v24, v56 offset0:64 offset1:96
	ds_write2_b32 v6, v25, v57 offset0:192 offset1:224
	ds_write2_b32 v7, v26, v58 offset0:64 offset1:96
	ds_write2_b32 v7, v27, v59 offset0:192 offset1:224
	ds_write2_b32 v8, v28, v60 offset0:64 offset1:96
	ds_write2_b32 v8, v29, v61 offset0:192 offset1:224
	ds_write2_b32 v9, v30, v62 offset0:64 offset1:96
	ds_write2_b32 v9, v31, v63 offset0:192 offset1:224
	ds_write2_b32 v10, v32, v64 offset0:64 offset1:96
	ds_write2_b32 v10, v33, v65 offset0:192 offset1:224
	ds_write2_b32 v11, v34, v66 offset0:64 offset1:96
	ds_write2_b32 v11, v35, v67 offset0:192 offset1:224
	ds_write2_b32 v12, v36, v68 offset0:64 offset1:96
	ds_write2_b32 v12, v37, v69 offset0:192 offset1:224
	s_andn2_b64 vcc, exec, s[10:11]
	s_waitcnt lgkmcnt(0)
	v_mov_b32_e32 v8, v114
	v_mov_b32_e32 v6, v113
	v_mov_b32_e32 v9, v112
	v_mov_b32_e32 v10, v111
	v_mov_b32_e32 v11, v110
	v_mov_b32_e32 v12, v109
	s_cbranch_vccz .LBB0_924
	s_branch .LBB0_921
